# ssm_pre conv tiles: both per-tile scalar kernarg pointer loads (xbcraw/xbcraw_c, act_cm_x/act_cm_c) replaced by selects between pointers loaded once before the tile loop
# speedup vs baseline: 1.0012x; 1.0012x over previous
; __device__ void ssm_pre_tile(KParams& p, int task, char* smem) {
;   const bool isx = task < 3072;
;   const int u = isx ? task : task - 3072;
;   const int ntt = isx ? 32 : 4;
;   const int ct = u % 24, tt = (u / 24) % ntt, b = u / (24 * ntt);
;   const int seqlen = isx ? L : CTX;
;   const bf16_t* raw = (isx ? p.xbcraw : p.xbcraw_c) + (size_t)b * seqlen * DXBC;
;   const int l0 = tt * 64, c0 = ct * 64, tid = threadIdx.x;
;   float (*rt)[68] = reinterpret_cast<float (*)[68]>(smem);
;   float (*at)[65] = reinterpret_cast<float (*)[65]>(smem + 66 * 68 * 4);
;   __syncthreads();
;   {
;     uint2 v[5];
; #pragma unroll
;     for (int k = 0; k < 5; ++k) {
;       const int i = tid + k * NTHREADS, r = i >> 4, c4 = i & 15, l = l0 - 1 + r;
;       v[k] = (i < 66 * 16 && l >= 0 && l < seqlen) ? *reinterpret_cast<const uint2*>(raw + (size_t)l * DXBC + c0 + c4 * 4) : uint2{0u, 0u};
;     }
; #pragma unroll
;     for (int k = 0; k < 5; ++k) {
;       const int i = tid + k * NTHREADS, r = i >> 4, c4 = i & 15;
;       if (i < 66 * 16) *reinterpret_cast<float4*>(&rt[r][c4 * 4]) = float4{bflo(v[k].x), bfhi(v[k].x), bflo(v[k].y), bfhi(v[k].y)};
;     }
;   }
;   __syncthreads();
;   {
;     const int cc = tid & 63, c = c0 + cc;
;     const float w0 = p.conv_w[c], w1 = p.conv_w[DXBC + c], w2 = p.conv_w[2 * DXBC + c], cb = p.conv_b[c];
; #pragma unroll 4
;     for (int r = tid >> 6; r < 64; r += 4) at[r][cc] = silu_f(cb + rt[r][cc] * w0 + rt[r + 1][cc] * w1 + rt[r + 2][cc] * w2);
;   }
;   __syncthreads();
;   const size_t trow0 = isx ? ((size_t)b * L + l0) : ((size_t)T + (size_t)b * CTX + l0);
; #pragma unroll
;   for (int k = 0; k < 4; ++k) {
;     const int i = tid + k * NTHREADS, r = i >> 4, c4 = (i & 15) * 4;
;     uint2 o; o.x = pack2(at[r][c4], at[r][c4 + 1]); o.y = pack2(at[r][c4 + 2], at[r][c4 + 3]);
;     *reinterpret_cast<uint2*>(p.act_tm + (trow0 + r) * DXBC + c0 + c4) = o;
;   }
;   if (c0 < 1280) {
;     bf16_t* cm = (isx ? p.act_cm_x : p.act_cm_c) + (size_t)b * 1280 * seqlen;
; #pragma unroll
;     for (int k = 0; k < 4; ++k) {
;       const int i = tid + k * NTHREADS, cc = i >> 4, r4 = (i & 15) * 4;
;       uint2 o; o.x = pack2(at[r4][cc], at[r4 + 1][cc]); o.y = pack2(at[r4 + 2][cc], at[r4 + 3][cc]);
;       *reinterpret_cast<uint2*>(cm + (size_t)(c0 + cc) * seqlen + l0 + r4) = o;
.LBB0_633:
	s_or_b64 exec, exec, s[10:11]
	s_cmpk_gt_i32 s2, 0xd7f
	s_cbranch_scc1 .LBB0_666
	v_or_b32_e32 v2, 0x100, v0
	s_load_dwordx4 s[16:19], s[14:15], 0x60
	s_load_dwordx4 s[60:63], s[14:15], 0x1b0
	s_load_dwordx4 s[72:75], s[14:15], 0x1f8
	s_load_dwordx2 s[20:21], s[14:15], 0x1f0
	v_lshrrev_b32_e32 v4, 4, v2
	v_or_b32_e32 v2, 0x200, v0
	v_lshlrev_b32_e32 v12, 2, v194
	s_movk_i32 s40, 0x110
	v_lshrrev_b32_e32 v6, 4, v2
	v_or_b32_e32 v2, 0x300, v0
	v_mad_u32_u24 v25, v192, s40, v12
	v_mul_i32_i24_e32 v13, -12, v192
	v_lshrrev_b32_e32 v8, 4, v2
	v_or_b32_e32 v2, 0x400, v0
	s_movk_i32 s12, 0x420
	v_mad_u32_u24 v26, v4, s40, v12
	v_mul_i32_i24_e32 v14, -12, v4
	v_add_u32_e32 v13, v25, v13
	s_waitcnt lgkmcnt(0)
	v_mov_b32_e32 v3, 0
	v_lshrrev_b32_e32 v24, 4, v2
	v_cmp_gt_u32_e64 s[12:13], s12, v2
	v_mad_u32_u24 v27, v6, s40, v12
	v_lshlrev_b32_e32 v2, 1, v194
	v_mul_i32_i24_e32 v15, -12, v6
	v_add_u32_e32 v35, 0x4620, v13
	v_add_u32_e32 v36, 0x4628, v13
	v_add_u32_e32 v13, v26, v14
	v_mad_u32_u24 v28, v8, s40, v12
	v_lshl_add_u64 v[10:11], s[20:21], 0, v[2:3]
	v_mul_i32_i24_e32 v16, -12, v8
	v_lshl_or_b32 v2, v194, 8, v12
	v_add_u32_e32 v37, 0x4620, v13
	v_add_u32_e32 v38, 0x4628, v13
	v_add_u32_e32 v13, v27, v15
	s_movk_i32 s6, 0x320
	s_movk_i32 s8, 0x220
	s_movk_i32 s10, 0x120
	v_mad_u32_u24 v29, v24, s40, v12
	v_lshl_add_u32 v12, v192, 2, v2
	v_lshl_add_u32 v17, v4, 2, v2
	v_lshl_add_u32 v18, v6, 2, v2
	v_lshl_add_u32 v19, v8, 2, v2
	v_mul_u32_u24_e32 v32, 0x104, v143
	s_movk_i32 s20, 0x4620
	v_add_u32_e32 v39, 0x4620, v13
	v_add_u32_e32 v40, 0x4628, v13
	v_add_u32_e32 v13, v28, v16
	v_cmp_gt_u32_e64 s[6:7], s6, v0
	v_cmp_gt_u32_e64 s[8:9], s8, v0
	v_cmp_gt_u32_e64 s[10:11], s10, v0
	v_mov_b32_e32 v193, v3
	v_mov_b32_e32 v5, v3
	v_mov_b32_e32 v7, v3
	v_mov_b32_e32 v9, v3
	v_mul_u32_u24_e32 v30, 0x110, v143
	v_mad_u32_u24 v31, v143, s40, v190
	s_movk_i32 s41, 0x104
	v_add3_u32 v33, v32, v190, s20
	v_add_u32_e32 v34, 0x4620, v190
	s_movk_i32 s42, 0xc00
	s_movk_i32 s43, 0x60
	s_movk_i32 s46, 0x800
	s_movk_i32 s47, 0x1b0
	v_lshlrev_b32_e32 v2, 1, v194
	s_mov_b64 s[20:21], 0
	v_add_u32_e32 v41, 0x4620, v13
	v_add_u32_e32 v42, 0x4628, v13
	s_movk_i32 s50, 0x1f8
	v_add_u32_e32 v43, 0x4400, v12
	v_add_u32_e32 v44, 0x4800, v12
	v_add_u32_e32 v45, 0x4400, v17
	v_add_u32_e32 v46, 0x4800, v17
	v_add_u32_e32 v47, 0x4400, v18
	v_add_u32_e32 v48, 0x4800, v18
	v_add_u32_e32 v49, 0x4400, v19
	v_add_u32_e32 v50, 0x4800, v19
	s_mov_b32 s51, s2
	s_branch .LBB0_636

; __device__ void ssm_pre_tile(KParams& p, int task, char* smem) {
;     ...
;   const size_t trow0 = isx ? ((size_t)b * L + l0) : ((size_t)T + (size_t)b * CTX + l0);
; #pragma unroll
;   for (int k = 0; k < 4; ++k) {
;     const int i = tid + k * NTHREADS, r = i >> 4, c4 = (i & 15) * 4;
;     uint2 o; o.x = pack2(at[r][c4], at[r][c4 + 1]); o.y = pack2(at[r][c4 + 2], at[r][c4 + 3]);
;     *reinterpret_cast<uint2*>(p.act_tm + (trow0 + r) * DXBC + c0 + c4) = o;
;   }
;   if (c0 < 1280) {
;     bf16_t* cm = (isx ? p.act_cm_x : p.act_cm_c) + (size_t)b * 1280 * seqlen;
; #pragma unroll
;     for (int k = 0; k < 4; ++k) {
;       const int i = tid + k * NTHREADS, cc = i >> 4, r4 = (i & 15) * 4;
;       uint2 o; o.x = pack2(at[r4][cc], at[r4 + 1][cc]); o.y = pack2(at[r4 + 2][cc], at[r4 + 3][cc]);
;       *reinterpret_cast<uint2*>(cm + (size_t)(c0 + cc) * seqlen + l0 + r4) = o;
;     }
;   }
.LBB0_661:
	ds_read2_b32 v[12:13], v35 offset1:1
	ds_read2_b32 v[14:15], v36 offset1:1
	v_lshl_add_u64 v[16:17], s[24:25], 1, v[10:11]
	ds_read2_b32 v[18:19], v37 offset1:1
	ds_read2_b32 v[20:21], v38 offset1:1
	s_cmp_gt_i32 s53, 19
	s_waitcnt lgkmcnt(3)
	v_cvt_pk_bf16_f32 v12, v12, v13
	s_waitcnt lgkmcnt(2)
	v_cvt_pk_bf16_f32 v13, v14, v15
	v_lshl_add_u64 v[14:15], s[30:31], 0, v[192:193]
	v_mad_u64_u32 v[22:23], s[36:37], v14, s42, v[16:17]
	v_mov_b32_e32 v14, v23
	v_mad_u64_u32 v[14:15], s[36:37], v15, s42, v[14:15]
	v_mov_b32_e32 v23, v14
	v_lshl_add_u64 v[14:15], s[30:31], 0, v[4:5]
	global_store_dwordx2 v[22:23], v[12:13], off
	s_waitcnt lgkmcnt(1)
	v_cvt_pk_bf16_f32 v12, v18, v19
	v_mad_u64_u32 v[18:19], s[36:37], v14, s42, v[16:17]
	v_mov_b32_e32 v14, v19
	v_mad_u64_u32 v[14:15], s[36:37], v15, s42, v[14:15]
	s_waitcnt lgkmcnt(0)
	v_cvt_pk_bf16_f32 v13, v20, v21
	v_mov_b32_e32 v19, v14
	ds_read2_b32 v[14:15], v39 offset1:1
	ds_read2_b32 v[20:21], v40 offset1:1
	global_store_dwordx2 v[18:19], v[12:13], off
	ds_read2_b32 v[12:13], v41 offset1:1
	ds_read2_b32 v[18:19], v42 offset1:1
	s_waitcnt lgkmcnt(3)
	v_cvt_pk_bf16_f32 v14, v14, v15
	s_waitcnt lgkmcnt(2)
	v_cvt_pk_bf16_f32 v15, v20, v21
	v_lshl_add_u64 v[20:21], s[30:31], 0, v[6:7]
	v_mad_u64_u32 v[22:23], s[36:37], v20, s42, v[16:17]
	v_mov_b32_e32 v20, v23
	v_mad_u64_u32 v[20:21], s[36:37], v21, s42, v[20:21]
	v_mov_b32_e32 v23, v20
	global_store_dwordx2 v[22:23], v[14:15], off
	v_lshl_add_u64 v[14:15], s[30:31], 0, v[8:9]
	v_mad_u64_u32 v[16:17], s[30:31], v14, s42, v[16:17]
	v_mov_b32_e32 v14, v17
	v_mad_u64_u32 v[14:15], s[30:31], v15, s42, v[14:15]
	s_waitcnt lgkmcnt(1)
	v_cvt_pk_bf16_f32 v12, v12, v13
	s_waitcnt lgkmcnt(0)
	v_cvt_pk_bf16_f32 v13, v18, v19
	v_mov_b32_e32 v17, v14
	global_store_dwordx2 v[16:17], v[12:13], off
	s_cbranch_scc1 .LBB0_635
	s_and_b64 s[22:23], s[22:23], exec
	s_cselect_b32 s22, s72, s74
	s_cselect_b32 s23, s73, s75
	s_mul_hi_i32 s27, s26, 0x500
	s_mulk_i32 s26, 0x500
	ds_read2_b32 v[12:13], v43 offset0:136 offset1:201
	ds_read2_b32 v[14:15], v44 offset0:10 offset1:75
	s_lshl_b64 s[26:27], s[26:27], s52
	s_lshl_b64 s[26:27], s[26:27], 1
	s_waitcnt lgkmcnt(0)
	s_add_u32 s25, s22, s26
	s_addc_u32 s26, s23, s27
	s_lshl_b64 s[22:23], s[28:29], 1
	s_add_u32 s22, s25, s22
	v_cvt_pk_bf16_f32 v12, v12, v13
	v_cvt_pk_bf16_f32 v13, v14, v15
	v_or_b32_e32 v14, s24, v192
	ds_read2_b32 v[18:19], v45 offset0:136 offset1:201
	ds_read2_b32 v[20:21], v46 offset0:10 offset1:75
	s_addc_u32 s23, s26, s23
	v_ashrrev_i32_e32 v15, 31, v14
	v_lshl_add_u64 v[16:17], s[22:23], 0, v[2:3]
	v_lshlrev_b64 v[14:15], s52, v[14:15]
	v_lshl_add_u64 v[14:15], v[14:15], 1, v[16:17]
	global_store_dwordx2 v[14:15], v[12:13], off
	v_add_u32_e32 v14, s24, v4
	s_waitcnt lgkmcnt(1)
	v_cvt_pk_bf16_f32 v12, v18, v19
	s_waitcnt lgkmcnt(0)
	v_cvt_pk_bf16_f32 v13, v20, v21
	v_ashrrev_i32_e32 v15, 31, v14
	ds_read2_b32 v[18:19], v47 offset0:136 offset1:201
	ds_read2_b32 v[20:21], v48 offset0:10 offset1:75
	v_lshlrev_b64 v[14:15], s52, v[14:15]
	v_lshl_add_u64 v[14:15], v[14:15], 1, v[16:17]
	global_store_dwordx2 v[14:15], v[12:13], off
	v_add_u32_e32 v14, s24, v6
	v_ashrrev_i32_e32 v15, 31, v14
	s_waitcnt lgkmcnt(1)
	v_cvt_pk_bf16_f32 v12, v18, v19
	s_waitcnt lgkmcnt(0)
	v_cvt_pk_bf16_f32 v13, v20, v21
	ds_read2_b32 v[18:19], v49 offset0:136 offset1:201
	ds_read2_b32 v[20:21], v50 offset0:10 offset1:75
	v_lshlrev_b64 v[14:15], s52, v[14:15]
	v_lshl_add_u64 v[14:15], v[14:15], 1, v[16:17]
	global_store_dwordx2 v[14:15], v[12:13], off
	v_add_u32_e32 v14, s24, v8
	v_ashrrev_i32_e32 v15, 31, v14
	v_lshlrev_b64 v[14:15], s52, v[14:15]
	s_waitcnt lgkmcnt(1)
	v_cvt_pk_bf16_f32 v12, v18, v19
	s_waitcnt lgkmcnt(0)
	v_cvt_pk_bf16_f32 v13, v20, v21
	v_lshl_add_u64 v[14:15], v[14:15], 1, v[16:17]
	global_store_dwordx2 v[14:15], v[12:13], off
	s_branch .LBB0_635
